# FFN-in tail: idle workgroups take 176/256 of the int8 strips instead of 197/256 (item share unchanged); on top of the kmean/gate-staging/barrier/QK-prefetch version
# speedup vs baseline: 1.0049x; 1.0004x over previous
.LBB0_121:
	v_readlane_b32 s0, v248, 11
	s_cmp_lt_u32 s0, 9
	v_readlane_b32 s0, v248, 17
	s_cselect_b32 s9, 0x108, 0
	s_cmp_lg_u32 s0, 0
	s_cselect_b64 s[0:1], -1, 0
	s_and_b64 s[10:11], s[0:1], exec
	s_cselect_b32 s9, s9, 0x100
	s_mul_i32 s10, s9, 0xb0
	s_lshr_b32 s10, s10, 8
	s_and_b64 s[4:5], s[4:5], exec
	s_cselect_b32 s4, 0, s10
	s_cselect_b32 s13, s10, s9
	s_add_i32 s14, s4, s8
	s_cmp_ge_i32 s14, s13
	s_cbranch_scc1 .LBB0_153
	s_lshl_b32 s4, s7, 14
	v_readlane_b32 s27, v248, 13
	s_add_i32 s15, s4, 0
	s_add_i32 s4, s27, 1
	s_mul_i32 s5, s4, 0xa400000
	v_readlane_b32 s8, v250, 34
	v_readlane_b32 s64, v250, 4
	s_add_u32 s8, s8, s5
	v_readlane_b32 s5, v250, 35
	v_readlane_b32 s65, v250, 5
	v_readlane_b32 s66, v250, 6
	v_readlane_b32 s67, v250, 7
	v_readlane_b32 s68, v250, 8
	v_readlane_b32 s69, v250, 9
	v_readlane_b32 s70, v250, 10
	v_readlane_b32 s71, v250, 11
	v_readlane_b32 s72, v250, 12
	v_readlane_b32 s73, v250, 13
	v_readlane_b32 s74, v250, 14
	v_readlane_b32 s75, v250, 15
	s_addc_u32 s9, s5, 0
	s_mul_i32 s4, s4, 0x2c00000
	s_mov_b32 s5, s60
	v_readlane_b32 s76, v250, 16
	v_readlane_b32 s77, v250, 17
	v_readlane_b32 s78, v250, 18
	v_readlane_b32 s79, v250, 19
	s_mov_b64 s[64:65], s[68:69]
	s_lshl_b64 s[4:5], s[4:5], 2
	s_mov_b64 s[66:67], s[70:71]
	s_mov_b64 s[68:69], s[72:73]
	s_mov_b64 s[70:71], s[74:75]
	s_add_u32 s4, s70, s4
	s_mul_i32 s26, s27, 0x6000
	s_addc_u32 s5, s71, s5
	s_add_i32 s10, s26, 0x6000
	s_add_u32 s24, s64, s10
	s_addc_u32 s25, s65, 0
	s_lshl_b32 s10, s7, 8
	s_ashr_i32 s11, s10, 31
	v_and_b32_e32 v4, 0xe0, v38
	s_lshl_b64 s[22:23], s[10:11], 2
	v_or_b32_e32 v6, s10, v4
	v_mov_b64_e32 v[8:9], s[4:5]
	s_mov_b32 s4, 0xb000
	s_add_u32 s24, s24, s22
	v_mad_i64_i32 v[8:9], s[4:5], v6, s4, v[8:9]
	s_addc_u32 s25, s25, s23
	s_lshl_b32 s4, s7, 7
	v_readlane_b32 s5, v249, 50
	s_add_i32 s4, s5, s4
	v_lshlrev_b32_e32 v2, 4, v37
	v_lshlrev_b32_e32 v10, 2, v112
	s_cmp_lt_u32 s6, 64
	v_mov_b32_e32 v11, v3
	v_cmp_gt_u32_e64 s[36:37], 8, v37
	v_add_u32_e32 v191, s4, v2
	v_add_u32_e32 v192, s5, v10
	s_cselect_b64 s[4:5], -1, 0
	v_lshl_add_u64 v[124:125], v[8:9], 0, v[10:11]
	s_and_b64 s[4:5], s[36:37], s[4:5]
	v_lshl_add_u64 v[8:9], s[8:9], 0, v[10:11]
	s_mov_b64 s[6:7], 0x2000000
	v_lshl_add_u64 v[126:127], v[8:9], 0, s[6:7]
	s_add_u32 s6, s8, s10
	s_mov_b64 s[72:73], s[76:77]
	s_mov_b64 s[74:75], s[78:79]
	v_readlane_b32 s76, v249, 55
	s_addc_u32 s7, s9, s11
	v_mov_b32_e32 v5, v3
	v_readlane_b32 s78, v249, 57
	v_lshl_add_u64 v[128:129], s[6:7], 0, v[4:5]
	s_lshl_b32 s6, s27, 24
	v_readlane_b32 s79, v249, 58
	v_ashrrev_i32_e32 v7, 31, v6
	s_add_u32 s6, s78, s6
	s_addc_u32 s7, s79, 0
	v_lshlrev_b64 v[8:9], 13, v[6:7]
	v_readlane_b32 s8, v248, 15
	v_lshl_add_u64 v[8:9], s[6:7], 0, v[8:9]
	v_readlane_b32 s9, v248, 16
	v_lshl_add_u64 v[130:131], v[8:9], 0, v[10:11]
	s_mov_b64 s[6:7], 0xa200000
	v_lshl_add_u64 v[8:9], s[8:9], 0, v[10:11]
	v_lshl_add_u64 v[132:133], v[8:9], 0, s[6:7]
	s_add_u32 s6, s8, s10
	s_addc_u32 s7, s9, s11
	v_lshl_add_u32 v190, v4, 2, s15
	v_lshl_add_u64 v[4:5], s[6:7], 0, v[4:5]
	s_mov_b64 s[6:7], 0x9c00000
	v_lshl_add_u64 v[134:135], v[4:5], 0, s[6:7]
	s_lshl_b32 s6, s27, 23
	v_readlane_b32 s77, v249, 56
	s_add_u32 s6, s76, s6
	s_addc_u32 s7, s77, 0
	s_lshl_b32 s8, s27, 13
	s_add_u32 s8, s68, s8
	s_addc_u32 s9, s69, 0
	s_add_u32 s8, s8, s22
	s_addc_u32 s9, s9, s23
	v_lshl_add_u64 v[136:137], s[8:9], 0, v[2:3]
	s_mul_i32 s8, s27, 0x2800000
	s_mul_hi_u32 s9, s27, 0x2800000
	s_add_u32 s8, s74, s8
	s_addc_u32 s9, s75, s9
	s_add_u32 s10, s64, s26
	s_addc_u32 s11, s65, 0
	s_add_u32 s10, s10, s22
	s_addc_u32 s11, s11, s23
	v_lshl_add_u64 v[12:13], s[10:11], 0, v[2:3]
	s_mov_b64 s[10:11], 0x2000
	v_lshl_add_u64 v[138:139], v[12:13], 0, s[10:11]
	v_mov_b64_e32 v[12:13], s[8:9]
	s_movk_i32 s8, 0x5000
	v_mad_i64_i32 v[12:13], s[8:9], v6, s8, v[12:13]
	s_mov_b64 s[8:9], 0x9400000
	v_readlane_b32 s80, v249, 59
	v_readlane_b32 s81, v249, 60
	v_lshl_add_u64 v[142:143], v[8:9], 0, s[8:9]
	s_mov_b64 s[8:9], 0x8400000
	v_readlane_b32 s72, v248, 9
	v_readlane_b32 s80, v248, 1
	v_readlane_b32 s78, v249, 63
	v_readlane_b32 s76, v250, 22
	v_readlane_b32 s26, v248, 5
	v_lshl_add_u64 v[144:145], v[4:5], 0, s[8:9]
	v_lshlrev_b64 v[4:5], 12, v[6:7]
	v_readlane_b32 s73, v248, 10
	v_readlane_b32 s82, v249, 61
	v_readlane_b32 s83, v249, 62
	v_readlane_b32 s81, v248, 2
	v_lshl_add_u64 v[122:123], s[24:25], 0, v[2:3]
	v_add_u32_e32 v113, s15, v2
	v_readlane_b32 s79, v248, 0
	v_readlane_b32 s77, v250, 23
	v_readlane_b32 s27, v248, 6
	v_lshl_add_u64 v[140:141], v[12:13], 0, v[10:11]
	v_lshl_add_u64 v[146:147], s[6:7], 0, v[4:5]
	s_lshl_b32 s6, s14, 5
	s_lshl_b32 s15, s12, 5
	s_branch .LBB0_125
